# speedup vs baseline: 1.0030x; 1.0030x over previous
_Z11prep_kernelPKfPKiS0_S0_S0_S0_PtS3_S3_P15HIP_vector_typeIfLj2EE:
	s_getpc_b64 s[34:35]
	s_load_dwordx8 s[8:15], s[0:1], 0x30
	s_cmpk_gt_i32 s2, 0x7ff
	s_mov_b64 s[4:5], -1
	s_cbranch_scc0 .LBB0_3
	v_lshl_or_b32 v1, s2, 8, v0
	v_add_u32_e32 v2, 0xfff80000, v1
	v_lshlrev_b32_e32 v1, 1, v0
	v_and_b32_e32 v1, 62, v1
	v_cvt_f64_u32_e32 v[4:5], v1
	v_ldexp_f64 v[4:5], -v[4:5], -6
	v_mov_b32_e32 v3, 0x40c38800
	v_mov_b32_e32 v1, 0x3ff00000
	v_cmp_eq_f64_e32 vcc, 0, v[4:5]
	v_mov_b32_e32 v6, 0
	s_mov_b32 s21, 0x3fe55555
	v_cndmask_b32_e32 v7, v3, v1, vcc
	v_frexp_mant_f64_e32 v[10:11], v[6:7]
	s_mov_b32 s20, 0x55555555
	v_cmp_gt_f64_e64 s[4:5], s[20:21], v[10:11]
	v_frexp_exp_i32_f64_e32 v3, v[6:7]
	s_load_dwordx2 s[6:7], s[0:1], 0x8
	v_cndmask_b32_e64 v7, 0, 1, s[4:5]
	v_ldexp_f64 v[10:11], v[10:11], v7
	v_add_f64 v[12:13], v[10:11], 1.0
	v_rcp_f64_e32 v[14:15], v[12:13]
	v_add_f64 v[18:19], v[12:13], -1.0
	v_add_f64 v[16:17], v[10:11], -1.0
	v_add_f64 v[10:11], v[10:11], -v[18:19]
	v_fma_f64 v[18:19], -v[12:13], v[14:15], 1.0
	v_fmac_f64_e32 v[14:15], v[18:19], v[14:15]
	v_fma_f64 v[18:19], -v[12:13], v[14:15], 1.0
	v_fmac_f64_e32 v[14:15], v[18:19], v[14:15]
	v_mul_f64 v[18:19], v[16:17], v[14:15]
	v_mul_f64 v[20:21], v[12:13], v[18:19]
	v_fma_f64 v[12:13], v[18:19], v[12:13], -v[20:21]
	v_fmac_f64_e32 v[12:13], v[18:19], v[10:11]
	v_add_f64 v[10:11], v[20:21], v[12:13]
	v_add_f64 v[22:23], v[16:17], -v[10:11]
	v_add_f64 v[20:21], v[10:11], -v[20:21]
	v_add_f64 v[16:17], v[16:17], -v[22:23]
	v_add_f64 v[10:11], v[16:17], -v[10:11]
	v_add_f64 v[12:13], v[20:21], -v[12:13]
	v_add_f64 v[10:11], v[12:13], v[10:11]
	v_add_f64 v[10:11], v[22:23], v[10:11]
	v_mul_f64 v[10:11], v[14:15], v[10:11]
	v_add_f64 v[12:13], v[18:19], v[10:11]
	v_add_f64 v[14:15], v[12:13], -v[18:19]
	v_add_f64 v[10:11], v[10:11], -v[14:15]
	v_mul_f64 v[14:15], v[12:13], v[12:13]
	v_fma_f64 v[16:17], v[12:13], v[12:13], -v[14:15]
	v_add_f64 v[18:19], v[10:11], v[10:11]
	v_fmac_f64_e32 v[16:17], v[12:13], v[18:19]
	v_subbrev_co_u32_e64 v3, s[4:5], 0, v3, s[4:5]
	v_add_f64 v[18:19], v[14:15], v[16:17]
	v_add_f64 v[14:15], v[18:19], -v[14:15]
	s_mov_b32 s4, 0x4222de17
	v_add_f64 v[14:15], v[16:17], -v[14:15]
	v_mov_b32_e32 v16, 0x968915a9
	v_mov_b32_e32 v17, 0x3fba6564
	s_mov_b32 s5, 0x3fbdee67
	v_fmac_f64_e32 v[16:17], s[4:5], v[18:19]
	v_mov_b32_e32 v20, 0x3abe935a
	v_mov_b32_e32 v21, 0x3fbe25e4
	v_fmac_f64_e32 v[20:21], v[18:19], v[16:17]
	v_mov_b32_e32 v16, 0x47e6c9c2
	v_mov_b32_e32 v17, 0x3fc110ef
	v_fmac_f64_e32 v[16:17], v[18:19], v[20:21]
	v_mov_b32_e32 v20, 0xcfa74449
	v_mov_b32_e32 v21, 0x3fc3b13b
	v_fmac_f64_e32 v[20:21], v[18:19], v[16:17]
	v_mov_b32_e32 v16, 0x71bf3c30
	v_mov_b32_e32 v17, 0x3fc745d1
	v_ashrrev_i32_e32 v8, 5, v2
	v_fmac_f64_e32 v[16:17], v[18:19], v[20:21]
	v_mov_b32_e32 v20, 0x1c7792ce
	v_mov_b32_e32 v21, 0x3fcc71c7
	v_fmac_f64_e32 v[20:21], v[18:19], v[16:17]
	v_mov_b32_e32 v16, 0x924920da
	v_mov_b32_e32 v17, 0x3fd24924
	v_ashrrev_i32_e32 v9, 31, v8
	v_fmac_f64_e32 v[16:17], v[18:19], v[20:21]
	v_mov_b32_e32 v20, 0x9999999c
	v_mov_b32_e32 v21, 0x3fd99999
	s_waitcnt lgkmcnt(0)
	v_lshl_add_u64 v[8:9], v[8:9], 2, s[6:7]
	v_fmac_f64_e32 v[20:21], v[18:19], v[16:17]
	v_cvt_f64_i32_e32 v[16:17], v3
	global_load_dword v3, v[8:9], off
	s_mov_b32 s17, 0x3fe62e42
	s_mov_b32 s16, 0xfefa39ef
	v_mul_f64 v[22:23], v[16:17], s[16:17]
	v_mul_f64 v[28:29], v[12:13], v[18:19]
	v_fma_f64 v[24:25], v[16:17], s[16:17], -v[22:23]
	s_mov_b32 s19, 0x3c7abc9e
	s_mov_b32 s18, 0x3b39803f
	v_fma_f64 v[30:31], v[18:19], v[12:13], -v[28:29]
	v_fmac_f64_e32 v[24:25], s[18:19], v[16:17]
	v_fmac_f64_e32 v[30:31], v[18:19], v[10:11]
	v_add_f64 v[16:17], v[22:23], v[24:25]
	v_fmac_f64_e32 v[30:31], v[14:15], v[12:13]
	v_add_f64 v[22:23], v[16:17], -v[22:23]
	v_ldexp_f64 v[26:27], v[10:11], 1
	v_add_f64 v[10:11], v[28:29], v[30:31]
	v_add_f64 v[22:23], v[24:25], -v[22:23]
	v_ldexp_f64 v[24:25], v[12:13], 1
	v_add_f64 v[12:13], v[10:11], -v[28:29]
	v_mul_f64 v[28:29], v[18:19], v[20:21]
	v_fma_f64 v[18:19], v[18:19], v[20:21], -v[28:29]
	v_fmac_f64_e32 v[18:19], v[14:15], v[20:21]
	v_add_f64 v[14:15], v[28:29], v[18:19]
	v_add_f64 v[20:21], v[14:15], -v[28:29]
	v_add_f64 v[18:19], v[18:19], -v[20:21]
	v_add_f64 v[20:21], v[14:15], s[20:21]
	s_mov_b32 s21, 0xbfe55555
	s_mov_b32 s4, 0xd5df274d
	v_add_f64 v[28:29], v[20:21], s[20:21]
	s_mov_b32 s5, 0x3c8543b0
	v_add_f64 v[14:15], v[14:15], -v[28:29]
	v_add_f64 v[18:19], v[18:19], s[4:5]
	v_add_f64 v[14:15], v[18:19], v[14:15]
	v_add_f64 v[18:19], v[20:21], v[14:15]
	v_add_f64 v[20:21], v[20:21], -v[18:19]
	v_add_f64 v[14:15], v[14:15], v[20:21]
	v_mul_f64 v[20:21], v[10:11], v[18:19]
	v_fma_f64 v[28:29], v[10:11], v[18:19], -v[20:21]
	v_add_f64 v[12:13], v[30:31], -v[12:13]
	v_fmac_f64_e32 v[28:29], v[10:11], v[14:15]
	v_fmac_f64_e32 v[28:29], v[12:13], v[18:19]
	v_add_f64 v[10:11], v[20:21], v[28:29]
	v_add_f64 v[12:13], v[10:11], -v[20:21]
	v_add_f64 v[14:15], v[24:25], v[10:11]
	v_add_f64 v[12:13], v[28:29], -v[12:13]
	v_add_f64 v[18:19], v[14:15], -v[24:25]
	v_add_f64 v[10:11], v[10:11], -v[18:19]
	v_add_f64 v[12:13], v[26:27], v[12:13]
	v_add_f64 v[10:11], v[12:13], v[10:11]
	v_add_f64 v[12:13], v[14:15], v[10:11]
	v_add_f64 v[14:15], v[12:13], -v[14:15]
	v_add_f64 v[10:11], v[10:11], -v[14:15]
	v_add_f64 v[14:15], v[16:17], v[12:13]
	v_add_f64 v[18:19], v[14:15], -v[16:17]
	v_add_f64 v[20:21], v[14:15], -v[18:19]
	v_add_f64 v[16:17], v[16:17], -v[20:21]
	v_add_f64 v[12:13], v[12:13], -v[18:19]
	v_add_f64 v[12:13], v[12:13], v[16:17]
	v_add_f64 v[16:17], v[22:23], v[10:11]
	v_add_f64 v[18:19], v[16:17], -v[22:23]
	v_add_f64 v[12:13], v[16:17], v[12:13]
	v_add_f64 v[20:21], v[16:17], -v[18:19]
	v_add_f64 v[16:17], v[14:15], v[12:13]
	v_add_f64 v[20:21], v[22:23], -v[20:21]
	v_add_f64 v[10:11], v[10:11], -v[18:19]
	v_add_f64 v[14:15], v[16:17], -v[14:15]
	v_add_f64 v[10:11], v[10:11], v[20:21]
	v_add_f64 v[12:13], v[12:13], -v[14:15]
	v_add_f64 v[10:11], v[10:11], v[12:13]
	v_add_f64 v[8:9], v[16:17], v[10:11]
	v_add_f64 v[12:13], v[8:9], -v[16:17]
	v_add_f64 v[10:11], v[10:11], -v[12:13]
	v_mul_f64 v[12:13], v[4:5], v[8:9]
	v_fma_f64 v[8:9], v[4:5], v[8:9], -v[12:13]
	v_fmac_f64_e32 v[8:9], v[4:5], v[10:11]
	s_movk_i32 s3, 0x204
	v_add_f64 v[10:11], v[12:13], v[8:9]
	v_cmp_class_f64_e64 s[4:5], v[12:13], s3
	s_mov_b32 s20, 0
	v_add_f64 v[14:15], v[10:11], -v[12:13]
	v_cndmask_b32_e64 v11, v11, v13, s[4:5]
	v_cndmask_b32_e64 v10, v10, v12, s[4:5]
	s_mov_b32 s21, 0x7ff00000
	v_add_f64 v[8:9], v[8:9], -v[14:15]
	v_cmp_neq_f64_e64 s[4:5], |v[10:11]|, s[20:21]
	s_mov_b32 s17, 0xbfe62e42
	s_mov_b32 s19, 0xbc7abc9e
	v_cndmask_b32_e64 v9, 0, v9, s[4:5]
	v_cndmask_b32_e64 v8, 0, v8, s[4:5]
	s_mov_b32 s4, 0x652b82fe
	s_mov_b32 s5, 0x3ff71547
	v_mul_f64 v[12:13], v[10:11], s[4:5]
	v_rndne_f64_e32 v[12:13], v[12:13]
	v_fma_f64 v[14:15], s[16:17], v[12:13], v[10:11]
	s_mov_b32 s4, 0x6a5dcb37
	v_fmac_f64_e32 v[14:15], s[18:19], v[12:13]
	v_mov_b32_e32 v16, 0xfca7ab0c
	v_mov_b32_e32 v17, 0x3e928af3
	s_mov_b32 s5, 0x3e5ade15
	v_fmac_f64_e32 v[16:17], s[4:5], v[14:15]
	v_mov_b32_e32 v18, 0x623fde64
	v_mov_b32_e32 v19, 0x3ec71dee
	v_fmac_f64_e32 v[18:19], v[14:15], v[16:17]
	v_mov_b32_e32 v16, 0x7c89e6b0
	v_mov_b32_e32 v17, 0x3efa0199
	v_fmac_f64_e32 v[16:17], v[14:15], v[18:19]
	v_mov_b32_e32 v18, 0x14761f6e
	v_mov_b32_e32 v19, 0x3f2a01a0
	v_fmac_f64_e32 v[18:19], v[14:15], v[16:17]
	v_mov_b32_e32 v16, 0x1852b7b0
	v_mov_b32_e32 v17, 0x3f56c16c
	v_fmac_f64_e32 v[16:17], v[14:15], v[18:19]
	v_mov_b32_e32 v18, 0x11122322
	v_mov_b32_e32 v19, 0x3f811111
	v_fmac_f64_e32 v[18:19], v[14:15], v[16:17]
	v_mov_b32_e32 v16, 0x555502a1
	v_mov_b32_e32 v17, 0x3fa55555
	v_fmac_f64_e32 v[16:17], v[14:15], v[18:19]
	v_mov_b32_e32 v18, 0x55555511
	v_mov_b32_e32 v19, 0x3fc55555
	v_fmac_f64_e32 v[18:19], v[14:15], v[16:17]
	v_mov_b32_e32 v16, 11
	v_mov_b32_e32 v17, 0x3fe00000
	v_fmac_f64_e32 v[16:17], v[14:15], v[18:19]
	v_fma_f64 v[16:17], v[14:15], v[16:17], 1.0
	s_mov_b32 s4, 0
	s_mov_b32 s6, 0
	v_fma_f64 v[14:15], v[14:15], v[16:17], 1.0
	v_cvt_i32_f64_e32 v7, v[12:13]
	s_mov_b32 s5, 0x40900000
	s_mov_b32 s7, 0xc090cc00
	v_ldexp_f64 v[12:13], v[14:15], v7
	v_mov_b32_e32 v7, 0x7ff00000
	v_cmp_nlt_f64_e64 s[4:5], s[4:5], v[10:11]
	v_cmp_ngt_f64_e64 s[6:7], s[6:7], v[10:11]
	s_waitcnt vmcnt(0)
	v_cvt_f32_i32_e32 v3, v3
	v_cndmask_b32_e64 v13, v7, v13, s[4:5]
	s_and_b64 s[4:5], s[6:7], s[4:5]
	v_cndmask_b32_e64 v11, 0, v13, s[6:7]
	v_cndmask_b32_e64 v10, 0, v12, s[4:5]
	v_mov_b64_e32 v[12:13], v[10:11]
	v_fmac_f64_e32 v[12:13], v[12:13], v[8:9]
	v_cmp_class_f64_e64 s[4:5], v[10:11], s3
	s_nop 1
	v_cndmask_b32_e64 v8, v13, v11, s[4:5]
	v_cndmask_b32_e64 v9, v12, v10, s[4:5]
	v_cmp_neq_f64_e64 s[4:5], v[4:5], |v[4:5]|
	v_and_b32_e32 v8, 0x7fffffff, v8
	s_nop 0
	v_cndmask_b32_e64 v7, v7, 0, s[4:5]
	v_cndmask_b32_e32 v7, v7, v1, vcc
	v_cmp_class_f64_e64 vcc, v[4:5], s3
	s_mov_b32 s4, 0
	s_mov_b32 s5, 0x41d00000
	v_cndmask_b32_e32 v5, v8, v7, vcc
	v_cndmask_b32_e64 v4, v9, 0, vcc
	v_cvt_f32_f64_e32 v4, v[4:5]
	v_mul_f32_e32 v3, v4, v3
	v_cvt_f64_f32_e32 v[4:5], v3
	v_cmp_nlt_f64_e64 s[6:7], |v[4:5]|, s[4:5]
	v_trig_preop_f64 v[16:17], |v[4:5]|, 0
	v_trig_preop_f64 v[14:15], |v[4:5]|, 1
	v_trig_preop_f64 v[12:13], |v[4:5]|, 2
	s_and_saveexec_b64 s[4:5], s[6:7]
	s_xor_b64 s[16:17], exec, s[4:5]
	s_cbranch_execz .LBB0_23
	s_mov_b32 s4, 0
	s_mov_b32 s5, 0x7b000000
	s_movk_i32 s3, 0xff80
	v_and_b32_e32 v3, 0x7fffffff, v5
	v_ldexp_f64 v[8:9], |v[4:5]|, s3
	v_cmp_ge_f64_e64 vcc, |v[4:5]|, s[4:5]
	s_mov_b32 s18, 0x33145c07
	s_mov_b32 s19, 0x3c91a626
	v_cndmask_b32_e32 v9, v3, v9, vcc
	v_cndmask_b32_e32 v8, v4, v8, vcc
	v_mul_f64 v[18:19], v[16:17], v[8:9]
	v_mul_f64 v[10:11], v[14:15], v[8:9]
	v_fma_f64 v[20:21], v[16:17], v[8:9], -v[18:19]
	v_add_f64 v[22:23], v[10:11], v[20:21]
	v_add_f64 v[30:31], v[22:23], -v[10:11]
	v_add_f64 v[20:21], v[20:21], -v[30:31]
	v_add_f64 v[30:31], v[22:23], -v[30:31]
	v_add_f64 v[30:31], v[10:11], -v[30:31]
	v_add_f64 v[20:21], v[20:21], v[30:31]
	v_fma_f64 v[10:11], v[14:15], v[8:9], -v[10:11]
	v_mul_f64 v[30:31], v[12:13], v[8:9]
	v_add_f64 v[32:33], v[30:31], v[10:11]
	v_add_f64 v[24:25], v[18:19], v[22:23]
	v_add_f64 v[34:35], v[32:33], v[20:21]
	v_ldexp_f64 v[26:27], v[24:25], -2
	v_add_f64 v[18:19], v[24:25], -v[18:19]
	v_add_f64 v[24:25], v[34:35], -v[32:33]
	v_add_f64 v[20:21], v[20:21], -v[24:25]
	v_add_f64 v[24:25], v[34:35], -v[24:25]
	v_add_f64 v[24:25], v[32:33], -v[24:25]
	v_add_f64 v[20:21], v[20:21], v[24:25]
	v_add_f64 v[24:25], v[32:33], -v[30:31]
	v_add_f64 v[10:11], v[10:11], -v[24:25]
	v_add_f64 v[24:25], v[32:33], -v[24:25]
	v_add_f64 v[24:25], v[30:31], -v[24:25]
	v_add_f64 v[18:19], v[22:23], -v[18:19]
	v_add_f64 v[10:11], v[10:11], v[24:25]
	v_fract_f64_e32 v[28:29], v[26:27]
	v_add_f64 v[22:23], v[18:19], v[34:35]
	v_add_f64 v[10:11], v[10:11], v[20:21]
	v_fma_f64 v[8:9], v[12:13], v[8:9], -v[30:31]
	v_add_f64 v[18:19], v[22:23], -v[18:19]
	v_add_f64 v[8:9], v[8:9], v[10:11]
	v_ldexp_f64 v[10:11], v[28:29], 2
	v_cmp_neq_f64_e64 vcc, |v[26:27]|, s[20:21]
	v_add_f64 v[18:19], v[34:35], -v[18:19]
	v_add_f64 v[8:9], v[18:19], v[8:9]
	v_cndmask_b32_e32 v11, 0, v11, vcc
	v_cndmask_b32_e32 v10, 0, v10, vcc
	v_add_f64 v[18:19], v[22:23], v[10:11]
	v_mov_b32_e32 v3, 0x40100000
	v_cmp_gt_f64_e32 vcc, 0, v[18:19]
	s_nop 1
	v_cndmask_b32_e32 v7, 0, v3, vcc
	v_add_f64 v[10:11], v[10:11], v[6:7]
	v_add_f64 v[18:19], v[22:23], v[10:11]
	v_cvt_i32_f64_e32 v3, v[18:19]
	v_cvt_f64_i32_e32 v[18:19], v3
	v_add_f64 v[10:11], v[10:11], -v[18:19]
	v_add_f64 v[18:19], v[22:23], v[10:11]
	v_add_f64 v[10:11], v[18:19], -v[10:11]
	v_cmp_le_f64_e32 vcc, 0.5, v[18:19]
	v_add_f64 v[10:11], v[22:23], -v[10:11]
	v_add_f64 v[8:9], v[8:9], v[10:11]
	v_addc_co_u32_e64 v3, s[4:5], 0, v3, vcc
	v_cndmask_b32_e32 v7, 0, v1, vcc
	v_add_f64 v[6:7], v[18:19], -v[6:7]
	s_mov_b32 s4, 0x54442d18
	v_add_f64 v[10:11], v[6:7], v[8:9]
	s_mov_b32 s5, 0x3ff921fb
	v_mul_f64 v[18:19], v[10:11], s[4:5]
	v_add_f64 v[6:7], v[10:11], -v[6:7]
	v_fma_f64 v[20:21], v[10:11], s[4:5], -v[18:19]
	v_add_f64 v[6:7], v[8:9], -v[6:7]
	v_fmac_f64_e32 v[20:21], s[18:19], v[10:11]
	v_fmac_f64_e32 v[20:21], s[4:5], v[6:7]
	v_add_f64 v[8:9], v[18:19], v[20:21]
	v_add_f64 v[6:7], v[8:9], -v[18:19]
	v_add_f64 v[10:11], v[20:21], -v[6:7]
	s_andn2_saveexec_b64 s[4:5], s[16:17]
	s_cbranch_execz .LBB0_25
	s_branch .LBB0_24
.LBB0_3:
	s_and_b64 vcc, exec, s[4:5]
	s_cbranch_vccz .LBB0_30
	s_load_dwordx2 s[4:5], s[0:1], 0x0
	s_load_dwordx8 s[16:23], s[0:1], 0x10
	s_ashr_i32 s3, s2, 31
	s_lshl_b64 s[0:1], s[2:3], 8
	v_or_b32_e32 v20, s0, v0
	v_mov_b32_e32 v21, s1
	s_mov_b64 s[0:1], 0xfffff
	v_cmp_lt_u64_e32 vcc, s[0:1], v[20:21]
	s_waitcnt lgkmcnt(0)
	s_lshr_b32 s36, s2, 3
	s_lshl_b32 s36, s36, 8
	s_cmp_lt_u32 s36, 0xe400
	s_cbranch_scc0 .Lpf_skip
	s_add_u32 s34, s34, s36
	s_addc_u32 s35, s35, 0
	s_load_dword s37, s[34:35], 0x0
	s_load_dword s37, s[34:35], 0x40
	s_load_dword s37, s[34:35], 0x80
	s_load_dword s37, s[34:35], 0xc0
.Lpf_skip:
	v_mov_b64_e32 v[18:19], s[8:9]
	v_mov_b64_e32 v[0:1], s[4:5]
	v_mov_b64_e32 v[16:17], v[20:21]
	s_and_saveexec_b64 s[2:3], vcc
	v_mov_b32_e32 v17, 0
	v_lshlrev_b64 v[0:1], 15, v[20:21]
	v_add_u32_e32 v1, -8, v1
	v_mov_b32_e32 v0, v17
	v_ashrrev_i64 v[0:1], 11, v[0:1]
	v_and_b32_e32 v16, 0x1ffff, v20
	v_lshl_add_u64 v[18:19], s[10:11], 0, v[0:1]
	v_mov_b64_e32 v[0:1], s[22:23]
	s_or_b64 exec, exec, s[2:3]
	v_lshlrev_b64 v[2:3], 5, v[16:17]
	v_lshl_add_u64 v[8:9], v[0:1], 0, v[2:3]
	global_load_dwordx4 v[0:3], v[8:9], off offset:16 nt
	global_load_dwordx4 v[4:7], v[8:9], off nt
	s_mov_b64 s[2:3], 0x80000
	v_lshl_add_u64 v[22:23], v[20:21], 0, s[2:3]
	v_cmp_lt_u64_e32 vcc, s[0:1], v[22:23]
	v_mov_b64_e32 v[8:9], s[4:5]
	v_mov_b64_e32 v[24:25], s[8:9]
	s_and_saveexec_b64 s[0:1], vcc
	s_cbranch_execz .LBB0_14
	s_mov_b32 s2, 0xfff80000
	s_mov_b32 s3, -1
	v_lshl_add_u64 v[10:11], v[20:21], 0, s[2:3]
	v_alignbit_b32 v12, v11, v10, 17
	v_cmp_lt_i32_e32 vcc, 0, v12
	s_mov_b64 s[2:3], 0
	s_and_saveexec_b64 s[6:7], vcc
	s_xor_b64 s[6:7], exec, s[6:7]
	s_cbranch_execz .LBB0_31
	v_cmp_eq_u32_e32 vcc, 1, v12
	s_mov_b64 s[2:3], -1
	s_and_saveexec_b64 s[14:15], vcc
	s_xor_b64 s[2:3], exec, -1
	s_or_b64 exec, exec, s[14:15]
	s_and_b64 s[2:3], s[2:3], exec
	s_or_saveexec_b64 s[6:7], s[6:7]
	v_mov_b64_e32 v[8:9], s[18:19]
	s_xor_b64 exec, exec, s[6:7]
	s_cbranch_execnz .LBB0_32

	.amdhsa_kernel _Z11prep_kernelPKfPKiS0_S0_S0_S0_PtS3_S3_P15HIP_vector_typeIfLj2EE
		.amdhsa_group_segment_fixed_size 0
		.amdhsa_private_segment_fixed_size 0
		.amdhsa_kernarg_size 80
		.amdhsa_user_sgpr_count 2
		.amdhsa_user_sgpr_dispatch_ptr 0
		.amdhsa_user_sgpr_queue_ptr 0
		.amdhsa_user_sgpr_kernarg_segment_ptr 1
		.amdhsa_user_sgpr_dispatch_id 0
		.amdhsa_user_sgpr_kernarg_preload_length 0
		.amdhsa_user_sgpr_kernarg_preload_offset 0
		.amdhsa_user_sgpr_private_segment_size 0
		.amdhsa_uses_dynamic_stack 0
		.amdhsa_enable_private_segment 0
		.amdhsa_system_sgpr_workgroup_id_x 1
		.amdhsa_system_sgpr_workgroup_id_y 0
		.amdhsa_system_sgpr_workgroup_id_z 0
		.amdhsa_system_sgpr_workgroup_info 0
		.amdhsa_system_vgpr_workitem_id 0
		.amdhsa_next_free_vgpr 40
		.amdhsa_next_free_sgpr 38
		.amdhsa_accum_offset 40
		.amdhsa_reserve_vcc 1
		.amdhsa_float_round_mode_32 0
		.amdhsa_float_round_mode_16_64 0
		.amdhsa_float_denorm_mode_32 3
		.amdhsa_float_denorm_mode_16_64 3
		.amdhsa_dx10_clamp 1
		.amdhsa_ieee_mode 1
		.amdhsa_fp16_overflow 0
		.amdhsa_tg_split 0
		.amdhsa_exception_fp_ieee_invalid_op 0
		.amdhsa_exception_fp_denorm_src 0
		.amdhsa_exception_fp_ieee_div_zero 0
		.amdhsa_exception_fp_ieee_overflow 0
		.amdhsa_exception_fp_ieee_underflow 0
		.amdhsa_exception_fp_ieee_inexact 0
		.amdhsa_exception_int_div_zero 0
	.end_amdhsa_kernel

amdhsa.kernels:
  - .agpr_count:     0
    .args:
      - .actual_access:  read_only
        .address_space:  global
        .offset:         0
        .size:           8
        .value_kind:     global_buffer
      - .actual_access:  read_only
        .address_space:  global
        .offset:         8
        .size:           8
        .value_kind:     global_buffer
      - .actual_access:  read_only
        .address_space:  global
        .offset:         16
        .size:           8
        .value_kind:     global_buffer
      - .actual_access:  read_only
        .address_space:  global
        .offset:         24
        .size:           8
        .value_kind:     global_buffer
      - .actual_access:  read_only
        .address_space:  global
        .offset:         32
        .size:           8
        .value_kind:     global_buffer
      - .actual_access:  read_only
        .address_space:  global
        .offset:         40
        .size:           8
        .value_kind:     global_buffer
      - .address_space:  global
        .offset:         48
        .size:           8
        .value_kind:     global_buffer
      - .address_space:  global
        .offset:         56
        .size:           8
        .value_kind:     global_buffer
      - .address_space:  global
        .offset:         64
        .size:           8
        .value_kind:     global_buffer
      - .address_space:  global
        .offset:         72
        .size:           8
        .value_kind:     global_buffer
    .group_segment_fixed_size: 0
    .kernarg_segment_align: 8
    .kernarg_segment_size: 80
    .language:       OpenCL C
    .language_version:
      - 2
      - 0
    .max_flat_workgroup_size: 256
    .name:           _Z11prep_kernelPKfPKiS0_S0_S0_S0_PtS3_S3_P15HIP_vector_typeIfLj2EE
    .private_segment_fixed_size: 0
    .sgpr_count:     44
    .sgpr_spill_count: 0
    .symbol:         _Z11prep_kernelPKfPKiS0_S0_S0_S0_PtS3_S3_P15HIP_vector_typeIfLj2EE.kd
    .uniform_work_group_size: 1
    .uses_dynamic_stack: false
    .vgpr_count:     40
    .vgpr_spill_count: 0
    .wavefront_size: 64
  - .agpr_count:     0
    .args:
      - .offset:         0
        .size:           32
        .value_kind:     by_value
      - .offset:         32
        .size:           24
        .value_kind:     by_value
      - .offset:         56
        .size:           32
        .value_kind:     by_value
      - .offset:         88
        .size:           24
        .value_kind:     by_value
      - .offset:         112
        .size:           4
        .value_kind:     hidden_block_count_x
      - .offset:         116
        .size:           4
        .value_kind:     hidden_block_count_y
      - .offset:         120
        .size:           4
        .value_kind:     hidden_block_count_z
      - .offset:         124
        .size:           2
        .value_kind:     hidden_group_size_x
      - .offset:         126
        .size:           2
        .value_kind:     hidden_group_size_y
      - .offset:         128
        .size:           2
        .value_kind:     hidden_group_size_z
      - .offset:         130
        .size:           2
        .value_kind:     hidden_remainder_x
      - .offset:         132
        .size:           2
        .value_kind:     hidden_remainder_y
      - .offset:         134
        .size:           2
        .value_kind:     hidden_remainder_z
      - .offset:         152
        .size:           8
        .value_kind:     hidden_global_offset_x
      - .offset:         160
        .size:           8
        .value_kind:     hidden_global_offset_y
      - .offset:         168
        .size:           8
        .value_kind:     hidden_global_offset_z
      - .offset:         176
        .size:           2
        .value_kind:     hidden_grid_dims
      - .offset:         232
        .size:           4
        .value_kind:     hidden_dynamic_lds_size
    .group_segment_fixed_size: 0
    .kernarg_segment_align: 8
    .kernarg_segment_size: 368
    .language:       OpenCL C
    .language_version:
      - 2
      - 0
    .max_flat_workgroup_size: 512
    .name:           _Z10qkv_kernelN3pg84GemmENS_7EpiRopeEN2hg4GemmENS2_7EpiRopeE
    .private_segment_fixed_size: 0
    .sgpr_count:     99
    .sgpr_spill_count: 0
    .symbol:         _Z10qkv_kernelN3pg84GemmENS_7EpiRopeEN2hg4GemmENS2_7EpiRopeE.kd
    .uniform_work_group_size: 1
    .uses_dynamic_stack: false
    .vgpr_count:     240
    .vgpr_spill_count: 0
    .wavefront_size: 64
  - .agpr_count:     0
    .args:
      - .address_space:  global
        .offset:         0
        .size:           8
        .value_kind:     global_buffer
      - .address_space:  global
        .offset:         8
        .size:           8
        .value_kind:     global_buffer
      - .address_space:  global
        .offset:         16
        .size:           8
        .value_kind:     global_buffer
      - .address_space:  global
        .offset:         24
        .size:           8
        .value_kind:     global_buffer
    .group_segment_fixed_size: 0
    .kernarg_segment_align: 8
    .kernarg_segment_size: 32
    .language:       OpenCL C
    .language_version:
      - 2
      - 0
    .max_flat_workgroup_size: 512
    .name:           _Z11attn_kernelPKDF16_S0_S0_PDF16_
    .private_segment_fixed_size: 0
    .sgpr_count:     62
    .sgpr_spill_count: 0
    .symbol:         _Z11attn_kernelPKDF16_S0_S0_PDF16_.kd
    .uniform_work_group_size: 1
    .uses_dynamic_stack: false
    .vgpr_count:     243
    .vgpr_spill_count: 0
    .wavefront_size: 64
  - .agpr_count:     0
    .args:
      - .offset:         0
        .size:           32
        .value_kind:     by_value
      - .offset:         32
        .size:           16
        .value_kind:     by_value
      - .offset:         48
        .size:           4
        .value_kind:     hidden_block_count_x
      - .offset:         52
        .size:           4
        .value_kind:     hidden_block_count_y
      - .offset:         56
        .size:           4
        .value_kind:     hidden_block_count_z
      - .offset:         60
        .size:           2
        .value_kind:     hidden_group_size_x
      - .offset:         62
        .size:           2
        .value_kind:     hidden_group_size_y
      - .offset:         64
        .size:           2
        .value_kind:     hidden_group_size_z
      - .offset:         66
        .size:           2
        .value_kind:     hidden_remainder_x
      - .offset:         68
        .size:           2
        .value_kind:     hidden_remainder_y
      - .offset:         70
        .size:           2
        .value_kind:     hidden_remainder_z
      - .offset:         88
        .size:           8
        .value_kind:     hidden_global_offset_x
      - .offset:         96
        .size:           8
        .value_kind:     hidden_global_offset_y
      - .offset:         104
        .size:           8
        .value_kind:     hidden_global_offset_z
      - .offset:         112
        .size:           2
        .value_kind:     hidden_grid_dims
      - .offset:         168
        .size:           4
        .value_kind:     hidden_dynamic_lds_size
    .group_segment_fixed_size: 0
    .kernarg_segment_align: 8
    .kernarg_segment_size: 304
    .language:       OpenCL C
    .language_version:
      - 2
      - 0
    .max_flat_workgroup_size: 512
    .name:           _Z12hgemm_kernelIN2hg6EpiF32EEvNS0_4GemmET_
    .private_segment_fixed_size: 0
    .sgpr_count:     62
    .sgpr_spill_count: 0
    .symbol:         _Z12hgemm_kernelIN2hg6EpiF32EEvNS0_4GemmET_.kd
    .uniform_work_group_size: 1
    .uses_dynamic_stack: false
    .vgpr_count:     138
    .vgpr_spill_count: 0
    .wavefront_size: 64
